# attention: disable the lagging-half PV deferral and its static priority (all 8 waves run QK/softmax/PV in step); outputs unchanged
# speedup vs baseline: 1.0070x; 1.0028x over previous
; __device__ __forceinline__ int opaque_tid() { int t = threadIdx.x; asm volatile("" : "+v"(t)); return t; }
; __device__ __forceinline__ void attn_unit(LAS unsigned char* lds, const unsigned char* Q, const unsigned char* KV, const bf16_t* KPE, const float* CST, bf16_t* O, int b, int h, int qb, CvtState& cs) {
;     const int tid = opaque_tid(), wid = __builtin_amdgcn_readfirstlane(tid >> 6), lane = tid & 63, r32 = lane & 31, hi = lane >> 5;
;     const bool lag = wid >= 4;
;     if (lag) __builtin_amdgcn_s_setprio(1);
.LBB0_1025:
	v_mov_b32_e32 v38, v0
	s_nop 0
	v_readfirstlane_b32 s24, v38
	s_ashr_i32 s33, s24, 6
	s_cmp_gt_i32 s33, 3
	s_mov_b64 s[38:39], 0
	s_cmp_lt_i32 s33, 4
	s_mov_b64 s[40:41], -1
	s_and_b64 vcc, exec, s[40:41]
	s_cbranch_vccnz .LBB0_1027
	s_setprio 1
